# K3 gather: barrier-free fast path (order-statistic classification in every wave) + 32-deep pipelined copy with scalar bases; slow path unchanged
# speedup vs baseline: 1.0073x; 1.0073x over previous
_Z20refine_gather_kernelPKfS0_S0_S0_S0_S0_S0_PfPiS1_:
	s_load_dwordx16 s[4:19], s[0:1], 0x0
	s_load_dwordx4 s[20:23], s[0:1], 0x40
	v_and_b32_e32 v1, 63, v0
	s_bfe_u32 s24, s2, 0x30003
	s_lshr_b32 s25, s2, 6
	s_lshl_b32 s25, s25, 2
	s_bfe_u32 s26, s2, 0x20001
	s_or_b32 s25, s25, s26
	s_and_b32 s26, s2, 1
	v_lshlrev_b32_e32 v2, 5, v1
	v_lshl_or_b32 v2, s24, 11, v2
	s_waitcnt lgkmcnt(0)
	s_load_dword s27, s[14:15], 0x0
	global_load_dwordx4 v[4:7], v2, s[16:17]
	global_load_dwordx4 v[8:11], v2, s[16:17] offset:16
	s_cmp_eq_u32 s26, 0
	s_cselect_b32 s30, s4, s6
	s_cselect_b32 s31, s5, s7
	s_lshl_b32 s32, s24, 5
	s_add_i32 s32, s32, s25
	s_lshl_b32 s32, s32, 18
	s_lshl_b32 s33, s26, 26
	s_or_b32 s32, s32, s33
	s_add_u32 s34, s22, s32
	s_addc_u32 s35, s23, 0
	v_mov_b32_e32 v18, 0
	v_mov_b32_e32 v19, 0x7f800000
	s_waitcnt vmcnt(0) lgkmcnt(0)
	v_add_f32_e32 v12, v4, v5
	v_add_f32_e32 v13, v6, v7
	v_add_f32_e32 v14, v8, v9
	v_add_f32_e32 v15, v10, v11
	v_add_f32_e32 v12, v12, v13
	v_add_f32_e32 v14, v14, v15
	v_add_f32_e32 v12, v12, v14
	v_mov_b32_e32 v3, s27
	v_fmamk_f32 v3, v12, 0x3c800000, v3
	v_add_f32_e32 v16, 0xba03126f, v3
	v_add_f32_e32 v17, 0x3a03126f, v3
	v_readlane_b32 s40, v3, 0
	v_readlane_b32 s41, v3, 1
	v_readlane_b32 s42, v3, 2
	v_readlane_b32 s43, v3, 3
	v_readlane_b32 s44, v3, 4
	v_readlane_b32 s45, v3, 5
	v_readlane_b32 s46, v3, 6
	v_readlane_b32 s47, v3, 7
	v_cmp_gt_f32_e64 s[48:49], s40, v3
	v_cmp_gt_f32_e64 s[50:51], s41, v3
	v_cmp_gt_f32_e64 s[52:53], s42, v3
	v_cmp_gt_f32_e64 s[54:55], s43, v3
	v_cmp_gt_f32_e64 s[56:57], s44, v3
	v_cmp_gt_f32_e64 s[58:59], s45, v3
	v_cmp_gt_f32_e64 s[60:61], s46, v3
	v_cmp_gt_f32_e64 s[62:63], s47, v3
	v_addc_co_u32_e64 v18, vcc, 0, v18, s[48:49]
	v_addc_co_u32_e64 v18, vcc, 0, v18, s[50:51]
	v_addc_co_u32_e64 v18, vcc, 0, v18, s[52:53]
	v_addc_co_u32_e64 v18, vcc, 0, v18, s[54:55]
	v_addc_co_u32_e64 v18, vcc, 0, v18, s[56:57]
	v_addc_co_u32_e64 v18, vcc, 0, v18, s[58:59]
	v_addc_co_u32_e64 v18, vcc, 0, v18, s[60:61]
	v_addc_co_u32_e64 v18, vcc, 0, v18, s[62:63]
	v_readlane_b32 s40, v3, 8
	v_readlane_b32 s41, v3, 9
	v_readlane_b32 s42, v3, 10
	v_readlane_b32 s43, v3, 11
	v_readlane_b32 s44, v3, 12
	v_readlane_b32 s45, v3, 13
	v_readlane_b32 s46, v3, 14
	v_readlane_b32 s47, v3, 15
	v_cmp_gt_f32_e64 s[48:49], s40, v3
	v_cmp_gt_f32_e64 s[50:51], s41, v3
	v_cmp_gt_f32_e64 s[52:53], s42, v3
	v_cmp_gt_f32_e64 s[54:55], s43, v3
	v_cmp_gt_f32_e64 s[56:57], s44, v3
	v_cmp_gt_f32_e64 s[58:59], s45, v3
	v_cmp_gt_f32_e64 s[60:61], s46, v3
	v_cmp_gt_f32_e64 s[62:63], s47, v3
	v_addc_co_u32_e64 v18, vcc, 0, v18, s[48:49]
	v_addc_co_u32_e64 v18, vcc, 0, v18, s[50:51]
	v_addc_co_u32_e64 v18, vcc, 0, v18, s[52:53]
	v_addc_co_u32_e64 v18, vcc, 0, v18, s[54:55]
	v_addc_co_u32_e64 v18, vcc, 0, v18, s[56:57]
	v_addc_co_u32_e64 v18, vcc, 0, v18, s[58:59]
	v_addc_co_u32_e64 v18, vcc, 0, v18, s[60:61]
	v_addc_co_u32_e64 v18, vcc, 0, v18, s[62:63]
	v_readlane_b32 s40, v3, 16
	v_readlane_b32 s41, v3, 17
	v_readlane_b32 s42, v3, 18
	v_readlane_b32 s43, v3, 19
	v_readlane_b32 s44, v3, 20
	v_readlane_b32 s45, v3, 21
	v_readlane_b32 s46, v3, 22
	v_readlane_b32 s47, v3, 23
	v_cmp_gt_f32_e64 s[48:49], s40, v3
	v_cmp_gt_f32_e64 s[50:51], s41, v3
	v_cmp_gt_f32_e64 s[52:53], s42, v3
	v_cmp_gt_f32_e64 s[54:55], s43, v3
	v_cmp_gt_f32_e64 s[56:57], s44, v3
	v_cmp_gt_f32_e64 s[58:59], s45, v3
	v_cmp_gt_f32_e64 s[60:61], s46, v3
	v_cmp_gt_f32_e64 s[62:63], s47, v3
	v_addc_co_u32_e64 v18, vcc, 0, v18, s[48:49]
	v_addc_co_u32_e64 v18, vcc, 0, v18, s[50:51]
	v_addc_co_u32_e64 v18, vcc, 0, v18, s[52:53]
	v_addc_co_u32_e64 v18, vcc, 0, v18, s[54:55]
	v_addc_co_u32_e64 v18, vcc, 0, v18, s[56:57]
	v_addc_co_u32_e64 v18, vcc, 0, v18, s[58:59]
	v_addc_co_u32_e64 v18, vcc, 0, v18, s[60:61]
	v_addc_co_u32_e64 v18, vcc, 0, v18, s[62:63]
	v_readlane_b32 s40, v3, 24
	v_readlane_b32 s41, v3, 25
	v_readlane_b32 s42, v3, 26
	v_readlane_b32 s43, v3, 27
	v_readlane_b32 s44, v3, 28
	v_readlane_b32 s45, v3, 29
	v_readlane_b32 s46, v3, 30
	v_readlane_b32 s47, v3, 31
	v_cmp_gt_f32_e64 s[48:49], s40, v3
	v_cmp_gt_f32_e64 s[50:51], s41, v3
	v_cmp_gt_f32_e64 s[52:53], s42, v3
	v_cmp_gt_f32_e64 s[54:55], s43, v3
	v_cmp_gt_f32_e64 s[56:57], s44, v3
	v_cmp_gt_f32_e64 s[58:59], s45, v3
	v_cmp_gt_f32_e64 s[60:61], s46, v3
	v_cmp_gt_f32_e64 s[62:63], s47, v3
	v_addc_co_u32_e64 v18, vcc, 0, v18, s[48:49]
	v_addc_co_u32_e64 v18, vcc, 0, v18, s[50:51]
	v_addc_co_u32_e64 v18, vcc, 0, v18, s[52:53]
	v_addc_co_u32_e64 v18, vcc, 0, v18, s[54:55]
	v_addc_co_u32_e64 v18, vcc, 0, v18, s[56:57]
	v_addc_co_u32_e64 v18, vcc, 0, v18, s[58:59]
	v_addc_co_u32_e64 v18, vcc, 0, v18, s[60:61]
	v_addc_co_u32_e64 v18, vcc, 0, v18, s[62:63]
	v_readlane_b32 s40, v3, 32
	v_readlane_b32 s41, v3, 33
	v_readlane_b32 s42, v3, 34
	v_readlane_b32 s43, v3, 35
	v_readlane_b32 s44, v3, 36
	v_readlane_b32 s45, v3, 37
	v_readlane_b32 s46, v3, 38
	v_readlane_b32 s47, v3, 39
	v_cmp_gt_f32_e64 s[48:49], s40, v3
	v_cmp_gt_f32_e64 s[50:51], s41, v3
	v_cmp_gt_f32_e64 s[52:53], s42, v3
	v_cmp_gt_f32_e64 s[54:55], s43, v3
	v_cmp_gt_f32_e64 s[56:57], s44, v3
	v_cmp_gt_f32_e64 s[58:59], s45, v3
	v_cmp_gt_f32_e64 s[60:61], s46, v3
	v_cmp_gt_f32_e64 s[62:63], s47, v3
	v_addc_co_u32_e64 v18, vcc, 0, v18, s[48:49]
	v_addc_co_u32_e64 v18, vcc, 0, v18, s[50:51]
	v_addc_co_u32_e64 v18, vcc, 0, v18, s[52:53]
	v_addc_co_u32_e64 v18, vcc, 0, v18, s[54:55]
	v_addc_co_u32_e64 v18, vcc, 0, v18, s[56:57]
	v_addc_co_u32_e64 v18, vcc, 0, v18, s[58:59]
	v_addc_co_u32_e64 v18, vcc, 0, v18, s[60:61]
	v_addc_co_u32_e64 v18, vcc, 0, v18, s[62:63]
	v_readlane_b32 s40, v3, 40
	v_readlane_b32 s41, v3, 41
	v_readlane_b32 s42, v3, 42
	v_readlane_b32 s43, v3, 43
	v_readlane_b32 s44, v3, 44
	v_readlane_b32 s45, v3, 45
	v_readlane_b32 s46, v3, 46
	v_readlane_b32 s47, v3, 47
	v_cmp_gt_f32_e64 s[48:49], s40, v3
	v_cmp_gt_f32_e64 s[50:51], s41, v3
	v_cmp_gt_f32_e64 s[52:53], s42, v3
	v_cmp_gt_f32_e64 s[54:55], s43, v3
	v_cmp_gt_f32_e64 s[56:57], s44, v3
	v_cmp_gt_f32_e64 s[58:59], s45, v3
	v_cmp_gt_f32_e64 s[60:61], s46, v3
	v_cmp_gt_f32_e64 s[62:63], s47, v3
	v_addc_co_u32_e64 v18, vcc, 0, v18, s[48:49]
	v_addc_co_u32_e64 v18, vcc, 0, v18, s[50:51]
	v_addc_co_u32_e64 v18, vcc, 0, v18, s[52:53]
	v_addc_co_u32_e64 v18, vcc, 0, v18, s[54:55]
	v_addc_co_u32_e64 v18, vcc, 0, v18, s[56:57]
	v_addc_co_u32_e64 v18, vcc, 0, v18, s[58:59]
	v_addc_co_u32_e64 v18, vcc, 0, v18, s[60:61]
	v_addc_co_u32_e64 v18, vcc, 0, v18, s[62:63]
	v_readlane_b32 s40, v3, 48
	v_readlane_b32 s41, v3, 49
	v_readlane_b32 s42, v3, 50
	v_readlane_b32 s43, v3, 51
	v_readlane_b32 s44, v3, 52
	v_readlane_b32 s45, v3, 53
	v_readlane_b32 s46, v3, 54
	v_readlane_b32 s47, v3, 55
	v_cmp_gt_f32_e64 s[48:49], s40, v3
	v_cmp_gt_f32_e64 s[50:51], s41, v3
	v_cmp_gt_f32_e64 s[52:53], s42, v3
	v_cmp_gt_f32_e64 s[54:55], s43, v3
	v_cmp_gt_f32_e64 s[56:57], s44, v3
	v_cmp_gt_f32_e64 s[58:59], s45, v3
	v_cmp_gt_f32_e64 s[60:61], s46, v3
	v_cmp_gt_f32_e64 s[62:63], s47, v3
	v_addc_co_u32_e64 v18, vcc, 0, v18, s[48:49]
	v_addc_co_u32_e64 v18, vcc, 0, v18, s[50:51]
	v_addc_co_u32_e64 v18, vcc, 0, v18, s[52:53]
	v_addc_co_u32_e64 v18, vcc, 0, v18, s[54:55]
	v_addc_co_u32_e64 v18, vcc, 0, v18, s[56:57]
	v_addc_co_u32_e64 v18, vcc, 0, v18, s[58:59]
	v_addc_co_u32_e64 v18, vcc, 0, v18, s[60:61]
	v_addc_co_u32_e64 v18, vcc, 0, v18, s[62:63]
	v_readlane_b32 s40, v3, 56
	v_readlane_b32 s41, v3, 57
	v_readlane_b32 s42, v3, 58
	v_readlane_b32 s43, v3, 59
	v_readlane_b32 s44, v3, 60
	v_readlane_b32 s45, v3, 61
	v_readlane_b32 s46, v3, 62
	v_readlane_b32 s47, v3, 63
	v_cmp_gt_f32_e64 s[48:49], s40, v3
	v_cmp_gt_f32_e64 s[50:51], s41, v3
	v_cmp_gt_f32_e64 s[52:53], s42, v3
	v_cmp_gt_f32_e64 s[54:55], s43, v3
	v_cmp_gt_f32_e64 s[56:57], s44, v3
	v_cmp_gt_f32_e64 s[58:59], s45, v3
	v_cmp_gt_f32_e64 s[60:61], s46, v3
	v_cmp_gt_f32_e64 s[62:63], s47, v3
	v_addc_co_u32_e64 v18, vcc, 0, v18, s[48:49]
	v_addc_co_u32_e64 v18, vcc, 0, v18, s[50:51]
	v_addc_co_u32_e64 v18, vcc, 0, v18, s[52:53]
	v_addc_co_u32_e64 v18, vcc, 0, v18, s[54:55]
	v_addc_co_u32_e64 v18, vcc, 0, v18, s[56:57]
	v_addc_co_u32_e64 v18, vcc, 0, v18, s[58:59]
	v_addc_co_u32_e64 v18, vcc, 0, v18, s[60:61]
	v_addc_co_u32_e64 v18, vcc, 0, v18, s[62:63]
	v_cmp_gt_u32_e64 s[48:49], 32, v18
	v_cmp_gt_u32_e64 s[50:51], 33, v18
	s_nop 1
	v_cndmask_b32_e64 v20, v19, v3, s[48:49]
	v_cndmask_b32_e64 v21, v19, v3, s[50:51]
	s_nop 1
	v_min_f32_dpp v20, v20, v20 quad_perm:[1,0,3,2] row_mask:0xf bank_mask:0xf
	v_min_f32_dpp v21, v21, v21 quad_perm:[1,0,3,2] row_mask:0xf bank_mask:0xf
	s_nop 1
	v_min_f32_dpp v20, v20, v20 quad_perm:[2,3,0,1] row_mask:0xf bank_mask:0xf
	v_min_f32_dpp v21, v21, v21 quad_perm:[2,3,0,1] row_mask:0xf bank_mask:0xf
	s_nop 1
	v_min_f32_dpp v20, v20, v20 row_half_mirror row_mask:0xf bank_mask:0xf
	v_min_f32_dpp v21, v21, v21 row_half_mirror row_mask:0xf bank_mask:0xf
	s_nop 1
	v_min_f32_dpp v20, v20, v20 row_mirror row_mask:0xf bank_mask:0xf
	v_min_f32_dpp v21, v21, v21 row_mirror row_mask:0xf bank_mask:0xf
	s_nop 1
	v_readlane_b32 s40, v20, 0
	v_readlane_b32 s41, v20, 16
	v_readlane_b32 s42, v20, 32
	v_readlane_b32 s43, v20, 48
	v_readlane_b32 s44, v21, 0
	v_readlane_b32 s45, v21, 16
	v_readlane_b32 s46, v21, 32
	v_readlane_b32 s47, v21, 48
	v_mov_b32_e32 v22, s40
	v_mov_b32_e32 v23, s44
	v_min_f32_e32 v22, s41, v22
	v_min_f32_e32 v23, s45, v23
	v_min_f32_e32 v22, s42, v22
	v_min_f32_e32 v23, s46, v23
	v_min_f32_e32 v22, s43, v22
	v_min_f32_e32 v23, s47, v23
	v_cmp_lt_f32_e64 s[50:51], v23, v16
	v_cmp_gt_f32_e64 s[52:53], v22, v17
	s_or_b64 s[54:55], s[50:51], s[52:53]
	s_not_b64 s[54:55], s[54:55]
	s_cbranch_scc1 .Lrg_slow
	v_mbcnt_lo_u32_b32 v22, s50, 0
	v_mbcnt_hi_u32_b32 v22, s51, v22
	v_cmp_eq_u32_e64 s[56:57], s25, v22
	s_and_b64 s[56:57], s[56:57], s[50:51]
	s_ff1_i32_b64 s28, s[56:57]
	s_lshl_b32 s29, s24, 6
	s_add_i32 s29, s29, s28
	s_lshl_b32 s29, s29, 18
	s_add_u32 s30, s30, s29
	s_addc_u32 s31, s31, 0
	v_lshlrev_b32_e32 v2, 4, v0
	global_load_dwordx4 v[4:7], v2, s[30:31] nt
	s_add_u32 s30, s30, 0x1000
	s_addc_u32 s31, s31, 0
	global_load_dwordx4 v[8:11], v2, s[30:31] nt
	s_add_u32 s30, s30, 0x1000
	s_addc_u32 s31, s31, 0
	global_load_dwordx4 v[12:15], v2, s[30:31] nt
	s_add_u32 s30, s30, 0x1000
	s_addc_u32 s31, s31, 0
	global_load_dwordx4 v[16:19], v2, s[30:31] nt
	s_add_u32 s30, s30, 0x1000
	s_addc_u32 s31, s31, 0
	global_load_dwordx4 v[20:23], v2, s[30:31] nt
	s_add_u32 s30, s30, 0x1000
	s_addc_u32 s31, s31, 0
	global_load_dwordx4 v[24:27], v2, s[30:31] nt
	s_add_u32 s30, s30, 0x1000
	s_addc_u32 s31, s31, 0
	global_load_dwordx4 v[28:31], v2, s[30:31] nt
	s_add_u32 s30, s30, 0x1000
	s_addc_u32 s31, s31, 0
	global_load_dwordx4 v[32:35], v2, s[30:31] nt
	s_add_u32 s30, s30, 0x1000
	s_addc_u32 s31, s31, 0
	global_load_dwordx4 v[36:39], v2, s[30:31] nt
	s_add_u32 s30, s30, 0x1000
	s_addc_u32 s31, s31, 0
	global_load_dwordx4 v[40:43], v2, s[30:31] nt
	s_add_u32 s30, s30, 0x1000
	s_addc_u32 s31, s31, 0
	global_load_dwordx4 v[44:47], v2, s[30:31] nt
	s_add_u32 s30, s30, 0x1000
	s_addc_u32 s31, s31, 0
	global_load_dwordx4 v[48:51], v2, s[30:31] nt
	s_add_u32 s30, s30, 0x1000
	s_addc_u32 s31, s31, 0
	global_load_dwordx4 v[52:55], v2, s[30:31] nt
	s_add_u32 s30, s30, 0x1000
	s_addc_u32 s31, s31, 0
	global_load_dwordx4 v[56:59], v2, s[30:31] nt
	s_add_u32 s30, s30, 0x1000
	s_addc_u32 s31, s31, 0
	global_load_dwordx4 v[60:63], v2, s[30:31] nt
	s_add_u32 s30, s30, 0x1000
	s_addc_u32 s31, s31, 0
	global_load_dwordx4 v[64:67], v2, s[30:31] nt
	s_add_u32 s30, s30, 0x1000
	s_addc_u32 s31, s31, 0
	global_load_dwordx4 v[68:71], v2, s[30:31] nt
	s_add_u32 s30, s30, 0x1000
	s_addc_u32 s31, s31, 0
	global_load_dwordx4 v[72:75], v2, s[30:31] nt
	s_add_u32 s30, s30, 0x1000
	s_addc_u32 s31, s31, 0
	global_load_dwordx4 v[76:79], v2, s[30:31] nt
	s_add_u32 s30, s30, 0x1000
	s_addc_u32 s31, s31, 0
	global_load_dwordx4 v[80:83], v2, s[30:31] nt
	s_add_u32 s30, s30, 0x1000
	s_addc_u32 s31, s31, 0
	global_load_dwordx4 v[84:87], v2, s[30:31] nt
	s_add_u32 s30, s30, 0x1000
	s_addc_u32 s31, s31, 0
	global_load_dwordx4 v[88:91], v2, s[30:31] nt
	s_add_u32 s30, s30, 0x1000
	s_addc_u32 s31, s31, 0
	global_load_dwordx4 v[92:95], v2, s[30:31] nt
	s_add_u32 s30, s30, 0x1000
	s_addc_u32 s31, s31, 0
	global_load_dwordx4 v[96:99], v2, s[30:31] nt
	s_add_u32 s30, s30, 0x1000
	s_addc_u32 s31, s31, 0
	global_load_dwordx4 v[100:103], v2, s[30:31] nt
	s_add_u32 s30, s30, 0x1000
	s_addc_u32 s31, s31, 0
	global_load_dwordx4 v[104:107], v2, s[30:31] nt
	s_add_u32 s30, s30, 0x1000
	s_addc_u32 s31, s31, 0
	global_load_dwordx4 v[108:111], v2, s[30:31] nt
	s_add_u32 s30, s30, 0x1000
	s_addc_u32 s31, s31, 0
	global_load_dwordx4 v[112:115], v2, s[30:31] nt
	s_add_u32 s30, s30, 0x1000
	s_addc_u32 s31, s31, 0
	global_load_dwordx4 v[116:119], v2, s[30:31] nt
	s_add_u32 s30, s30, 0x1000
	s_addc_u32 s31, s31, 0
	global_load_dwordx4 v[120:123], v2, s[30:31] nt
	s_add_u32 s30, s30, 0x1000
	s_addc_u32 s31, s31, 0
	global_load_dwordx4 v[124:127], v2, s[30:31] nt
	s_add_u32 s30, s30, 0x1000
	s_addc_u32 s31, s31, 0
	global_load_dwordx4 v[128:131], v2, s[30:31] nt
	s_add_u32 s30, s30, 0x1000
	s_addc_u32 s31, s31, 0
	s_waitcnt vmcnt(31)
	global_store_dwordx4 v2, v[4:7], s[34:35] nt
	s_add_u32 s34, s34, 0x1000
	s_addc_u32 s35, s35, 0
	global_load_dwordx4 v[4:7], v2, s[30:31] nt
	s_add_u32 s30, s30, 0x1000
	s_addc_u32 s31, s31, 0
	s_waitcnt vmcnt(32)
	global_store_dwordx4 v2, v[8:11], s[34:35] nt
	s_add_u32 s34, s34, 0x1000
	s_addc_u32 s35, s35, 0
	global_load_dwordx4 v[8:11], v2, s[30:31] nt
	s_add_u32 s30, s30, 0x1000
	s_addc_u32 s31, s31, 0
	s_waitcnt vmcnt(33)
	global_store_dwordx4 v2, v[12:15], s[34:35] nt
	s_add_u32 s34, s34, 0x1000
	s_addc_u32 s35, s35, 0
	global_load_dwordx4 v[12:15], v2, s[30:31] nt
	s_add_u32 s30, s30, 0x1000
	s_addc_u32 s31, s31, 0
	s_waitcnt vmcnt(34)
	global_store_dwordx4 v2, v[16:19], s[34:35] nt
	s_add_u32 s34, s34, 0x1000
	s_addc_u32 s35, s35, 0
	global_load_dwordx4 v[16:19], v2, s[30:31] nt
	s_add_u32 s30, s30, 0x1000
	s_addc_u32 s31, s31, 0
	s_waitcnt vmcnt(35)
	global_store_dwordx4 v2, v[20:23], s[34:35] nt
	s_add_u32 s34, s34, 0x1000
	s_addc_u32 s35, s35, 0
	global_load_dwordx4 v[20:23], v2, s[30:31] nt
	s_add_u32 s30, s30, 0x1000
	s_addc_u32 s31, s31, 0
	s_waitcnt vmcnt(36)
	global_store_dwordx4 v2, v[24:27], s[34:35] nt
	s_add_u32 s34, s34, 0x1000
	s_addc_u32 s35, s35, 0
	global_load_dwordx4 v[24:27], v2, s[30:31] nt
	s_add_u32 s30, s30, 0x1000
	s_addc_u32 s31, s31, 0
	s_waitcnt vmcnt(37)
	global_store_dwordx4 v2, v[28:31], s[34:35] nt
	s_add_u32 s34, s34, 0x1000
	s_addc_u32 s35, s35, 0
	global_load_dwordx4 v[28:31], v2, s[30:31] nt
	s_add_u32 s30, s30, 0x1000
	s_addc_u32 s31, s31, 0
	s_waitcnt vmcnt(38)
	global_store_dwordx4 v2, v[32:35], s[34:35] nt
	s_add_u32 s34, s34, 0x1000
	s_addc_u32 s35, s35, 0
	global_load_dwordx4 v[32:35], v2, s[30:31] nt
	s_add_u32 s30, s30, 0x1000
	s_addc_u32 s31, s31, 0
	s_waitcnt vmcnt(39)
	global_store_dwordx4 v2, v[36:39], s[34:35] nt
	s_add_u32 s34, s34, 0x1000
	s_addc_u32 s35, s35, 0
	global_load_dwordx4 v[36:39], v2, s[30:31] nt
	s_add_u32 s30, s30, 0x1000
	s_addc_u32 s31, s31, 0
	s_waitcnt vmcnt(40)
	global_store_dwordx4 v2, v[40:43], s[34:35] nt
	s_add_u32 s34, s34, 0x1000
	s_addc_u32 s35, s35, 0
	global_load_dwordx4 v[40:43], v2, s[30:31] nt
	s_add_u32 s30, s30, 0x1000
	s_addc_u32 s31, s31, 0
	s_waitcnt vmcnt(41)
	global_store_dwordx4 v2, v[44:47], s[34:35] nt
	s_add_u32 s34, s34, 0x1000
	s_addc_u32 s35, s35, 0
	global_load_dwordx4 v[44:47], v2, s[30:31] nt
	s_add_u32 s30, s30, 0x1000
	s_addc_u32 s31, s31, 0
	s_waitcnt vmcnt(42)
	global_store_dwordx4 v2, v[48:51], s[34:35] nt
	s_add_u32 s34, s34, 0x1000
	s_addc_u32 s35, s35, 0
	global_load_dwordx4 v[48:51], v2, s[30:31] nt
	s_add_u32 s30, s30, 0x1000
	s_addc_u32 s31, s31, 0
	s_waitcnt vmcnt(43)
	global_store_dwordx4 v2, v[52:55], s[34:35] nt
	s_add_u32 s34, s34, 0x1000
	s_addc_u32 s35, s35, 0
	global_load_dwordx4 v[52:55], v2, s[30:31] nt
	s_add_u32 s30, s30, 0x1000
	s_addc_u32 s31, s31, 0
	s_waitcnt vmcnt(44)
	global_store_dwordx4 v2, v[56:59], s[34:35] nt
	s_add_u32 s34, s34, 0x1000
	s_addc_u32 s35, s35, 0
	global_load_dwordx4 v[56:59], v2, s[30:31] nt
	s_add_u32 s30, s30, 0x1000
	s_addc_u32 s31, s31, 0
	s_waitcnt vmcnt(45)
	global_store_dwordx4 v2, v[60:63], s[34:35] nt
	s_add_u32 s34, s34, 0x1000
	s_addc_u32 s35, s35, 0
	global_load_dwordx4 v[60:63], v2, s[30:31] nt
	s_add_u32 s30, s30, 0x1000
	s_addc_u32 s31, s31, 0
	s_waitcnt vmcnt(46)
	global_store_dwordx4 v2, v[64:67], s[34:35] nt
	s_add_u32 s34, s34, 0x1000
	s_addc_u32 s35, s35, 0
	global_load_dwordx4 v[64:67], v2, s[30:31] nt
	s_add_u32 s30, s30, 0x1000
	s_addc_u32 s31, s31, 0
	s_waitcnt vmcnt(47)
	global_store_dwordx4 v2, v[68:71], s[34:35] nt
	s_add_u32 s34, s34, 0x1000
	s_addc_u32 s35, s35, 0
	global_load_dwordx4 v[68:71], v2, s[30:31] nt
	s_add_u32 s30, s30, 0x1000
	s_addc_u32 s31, s31, 0
	s_waitcnt vmcnt(48)
	global_store_dwordx4 v2, v[72:75], s[34:35] nt
	s_add_u32 s34, s34, 0x1000
	s_addc_u32 s35, s35, 0
	global_load_dwordx4 v[72:75], v2, s[30:31] nt
	s_add_u32 s30, s30, 0x1000
	s_addc_u32 s31, s31, 0
	s_waitcnt vmcnt(49)
	global_store_dwordx4 v2, v[76:79], s[34:35] nt
	s_add_u32 s34, s34, 0x1000
	s_addc_u32 s35, s35, 0
	global_load_dwordx4 v[76:79], v2, s[30:31] nt
	s_add_u32 s30, s30, 0x1000
	s_addc_u32 s31, s31, 0
	s_waitcnt vmcnt(50)
	global_store_dwordx4 v2, v[80:83], s[34:35] nt
	s_add_u32 s34, s34, 0x1000
	s_addc_u32 s35, s35, 0
	global_load_dwordx4 v[80:83], v2, s[30:31] nt
	s_add_u32 s30, s30, 0x1000
	s_addc_u32 s31, s31, 0
	s_waitcnt vmcnt(51)
	global_store_dwordx4 v2, v[84:87], s[34:35] nt
	s_add_u32 s34, s34, 0x1000
	s_addc_u32 s35, s35, 0
	global_load_dwordx4 v[84:87], v2, s[30:31] nt
	s_add_u32 s30, s30, 0x1000
	s_addc_u32 s31, s31, 0
	s_waitcnt vmcnt(52)
	global_store_dwordx4 v2, v[88:91], s[34:35] nt
	s_add_u32 s34, s34, 0x1000
	s_addc_u32 s35, s35, 0
	global_load_dwordx4 v[88:91], v2, s[30:31] nt
	s_add_u32 s30, s30, 0x1000
	s_addc_u32 s31, s31, 0
	s_waitcnt vmcnt(53)
	global_store_dwordx4 v2, v[92:95], s[34:35] nt
	s_add_u32 s34, s34, 0x1000
	s_addc_u32 s35, s35, 0
	global_load_dwordx4 v[92:95], v2, s[30:31] nt
	s_add_u32 s30, s30, 0x1000
	s_addc_u32 s31, s31, 0
	s_waitcnt vmcnt(54)
	global_store_dwordx4 v2, v[96:99], s[34:35] nt
	s_add_u32 s34, s34, 0x1000
	s_addc_u32 s35, s35, 0
	global_load_dwordx4 v[96:99], v2, s[30:31] nt
	s_add_u32 s30, s30, 0x1000
	s_addc_u32 s31, s31, 0
	s_waitcnt vmcnt(55)
	global_store_dwordx4 v2, v[100:103], s[34:35] nt
	s_add_u32 s34, s34, 0x1000
	s_addc_u32 s35, s35, 0
	global_load_dwordx4 v[100:103], v2, s[30:31] nt
	s_add_u32 s30, s30, 0x1000
	s_addc_u32 s31, s31, 0
	s_waitcnt vmcnt(56)
	global_store_dwordx4 v2, v[104:107], s[34:35] nt
	s_add_u32 s34, s34, 0x1000
	s_addc_u32 s35, s35, 0
	global_load_dwordx4 v[104:107], v2, s[30:31] nt
	s_add_u32 s30, s30, 0x1000
	s_addc_u32 s31, s31, 0
	s_waitcnt vmcnt(57)
	global_store_dwordx4 v2, v[108:111], s[34:35] nt
	s_add_u32 s34, s34, 0x1000
	s_addc_u32 s35, s35, 0
	global_load_dwordx4 v[108:111], v2, s[30:31] nt
	s_add_u32 s30, s30, 0x1000
	s_addc_u32 s31, s31, 0
	s_waitcnt vmcnt(58)
	global_store_dwordx4 v2, v[112:115], s[34:35] nt
	s_add_u32 s34, s34, 0x1000
	s_addc_u32 s35, s35, 0
	global_load_dwordx4 v[112:115], v2, s[30:31] nt
	s_add_u32 s30, s30, 0x1000
	s_addc_u32 s31, s31, 0
	s_waitcnt vmcnt(59)
	global_store_dwordx4 v2, v[116:119], s[34:35] nt
	s_add_u32 s34, s34, 0x1000
	s_addc_u32 s35, s35, 0
	global_load_dwordx4 v[116:119], v2, s[30:31] nt
	s_add_u32 s30, s30, 0x1000
	s_addc_u32 s31, s31, 0
	s_waitcnt vmcnt(60)
	global_store_dwordx4 v2, v[120:123], s[34:35] nt
	s_add_u32 s34, s34, 0x1000
	s_addc_u32 s35, s35, 0
	global_load_dwordx4 v[120:123], v2, s[30:31] nt
	s_add_u32 s30, s30, 0x1000
	s_addc_u32 s31, s31, 0
	s_waitcnt vmcnt(61)
	global_store_dwordx4 v2, v[124:127], s[34:35] nt
	s_add_u32 s34, s34, 0x1000
	s_addc_u32 s35, s35, 0
	global_load_dwordx4 v[124:127], v2, s[30:31] nt
	s_add_u32 s30, s30, 0x1000
	s_addc_u32 s31, s31, 0
	s_waitcnt vmcnt(62)
	global_store_dwordx4 v2, v[128:131], s[34:35] nt
	s_add_u32 s34, s34, 0x1000
	s_addc_u32 s35, s35, 0
	global_load_dwordx4 v[128:131], v2, s[30:31] nt
	s_add_u32 s30, s30, 0x1000
	s_addc_u32 s31, s31, 0
	s_waitcnt vmcnt(62)
	global_store_dwordx4 v2, v[4:7], s[34:35] nt
	s_add_u32 s34, s34, 0x1000
	s_addc_u32 s35, s35, 0
	s_waitcnt vmcnt(61)
	global_store_dwordx4 v2, v[8:11], s[34:35] nt
	s_add_u32 s34, s34, 0x1000
	s_addc_u32 s35, s35, 0
	s_waitcnt vmcnt(60)
	global_store_dwordx4 v2, v[12:15], s[34:35] nt
	s_add_u32 s34, s34, 0x1000
	s_addc_u32 s35, s35, 0
	s_waitcnt vmcnt(59)
	global_store_dwordx4 v2, v[16:19], s[34:35] nt
	s_add_u32 s34, s34, 0x1000
	s_addc_u32 s35, s35, 0
	s_waitcnt vmcnt(58)
	global_store_dwordx4 v2, v[20:23], s[34:35] nt
	s_add_u32 s34, s34, 0x1000
	s_addc_u32 s35, s35, 0
	s_waitcnt vmcnt(57)
	global_store_dwordx4 v2, v[24:27], s[34:35] nt
	s_add_u32 s34, s34, 0x1000
	s_addc_u32 s35, s35, 0
	s_waitcnt vmcnt(56)
	global_store_dwordx4 v2, v[28:31], s[34:35] nt
	s_add_u32 s34, s34, 0x1000
	s_addc_u32 s35, s35, 0
	s_waitcnt vmcnt(55)
	global_store_dwordx4 v2, v[32:35], s[34:35] nt
	s_add_u32 s34, s34, 0x1000
	s_addc_u32 s35, s35, 0
	s_waitcnt vmcnt(54)
	global_store_dwordx4 v2, v[36:39], s[34:35] nt
	s_add_u32 s34, s34, 0x1000
	s_addc_u32 s35, s35, 0
	s_waitcnt vmcnt(53)
	global_store_dwordx4 v2, v[40:43], s[34:35] nt
	s_add_u32 s34, s34, 0x1000
	s_addc_u32 s35, s35, 0
	s_waitcnt vmcnt(52)
	global_store_dwordx4 v2, v[44:47], s[34:35] nt
	s_add_u32 s34, s34, 0x1000
	s_addc_u32 s35, s35, 0
	s_waitcnt vmcnt(51)
	global_store_dwordx4 v2, v[48:51], s[34:35] nt
	s_add_u32 s34, s34, 0x1000
	s_addc_u32 s35, s35, 0
	s_waitcnt vmcnt(50)
	global_store_dwordx4 v2, v[52:55], s[34:35] nt
	s_add_u32 s34, s34, 0x1000
	s_addc_u32 s35, s35, 0
	s_waitcnt vmcnt(49)
	global_store_dwordx4 v2, v[56:59], s[34:35] nt
	s_add_u32 s34, s34, 0x1000
	s_addc_u32 s35, s35, 0
	s_waitcnt vmcnt(48)
	global_store_dwordx4 v2, v[60:63], s[34:35] nt
	s_add_u32 s34, s34, 0x1000
	s_addc_u32 s35, s35, 0
	s_waitcnt vmcnt(47)
	global_store_dwordx4 v2, v[64:67], s[34:35] nt
	s_add_u32 s34, s34, 0x1000
	s_addc_u32 s35, s35, 0
	s_waitcnt vmcnt(46)
	global_store_dwordx4 v2, v[68:71], s[34:35] nt
	s_add_u32 s34, s34, 0x1000
	s_addc_u32 s35, s35, 0
	s_waitcnt vmcnt(45)
	global_store_dwordx4 v2, v[72:75], s[34:35] nt
	s_add_u32 s34, s34, 0x1000
	s_addc_u32 s35, s35, 0
	s_waitcnt vmcnt(44)
	global_store_dwordx4 v2, v[76:79], s[34:35] nt
	s_add_u32 s34, s34, 0x1000
	s_addc_u32 s35, s35, 0
	s_waitcnt vmcnt(43)
	global_store_dwordx4 v2, v[80:83], s[34:35] nt
	s_add_u32 s34, s34, 0x1000
	s_addc_u32 s35, s35, 0
	s_waitcnt vmcnt(42)
	global_store_dwordx4 v2, v[84:87], s[34:35] nt
	s_add_u32 s34, s34, 0x1000
	s_addc_u32 s35, s35, 0
	s_waitcnt vmcnt(41)
	global_store_dwordx4 v2, v[88:91], s[34:35] nt
	s_add_u32 s34, s34, 0x1000
	s_addc_u32 s35, s35, 0
	s_waitcnt vmcnt(40)
	global_store_dwordx4 v2, v[92:95], s[34:35] nt
	s_add_u32 s34, s34, 0x1000
	s_addc_u32 s35, s35, 0
	s_waitcnt vmcnt(39)
	global_store_dwordx4 v2, v[96:99], s[34:35] nt
	s_add_u32 s34, s34, 0x1000
	s_addc_u32 s35, s35, 0
	s_waitcnt vmcnt(38)
	global_store_dwordx4 v2, v[100:103], s[34:35] nt
	s_add_u32 s34, s34, 0x1000
	s_addc_u32 s35, s35, 0
	s_waitcnt vmcnt(37)
	global_store_dwordx4 v2, v[104:107], s[34:35] nt
	s_add_u32 s34, s34, 0x1000
	s_addc_u32 s35, s35, 0
	s_waitcnt vmcnt(36)
	global_store_dwordx4 v2, v[108:111], s[34:35] nt
	s_add_u32 s34, s34, 0x1000
	s_addc_u32 s35, s35, 0
	s_waitcnt vmcnt(35)
	global_store_dwordx4 v2, v[112:115], s[34:35] nt
	s_add_u32 s34, s34, 0x1000
	s_addc_u32 s35, s35, 0
	s_waitcnt vmcnt(34)
	global_store_dwordx4 v2, v[116:119], s[34:35] nt
	s_add_u32 s34, s34, 0x1000
	s_addc_u32 s35, s35, 0
	s_waitcnt vmcnt(33)
	global_store_dwordx4 v2, v[120:123], s[34:35] nt
	s_add_u32 s34, s34, 0x1000
	s_addc_u32 s35, s35, 0
	s_waitcnt vmcnt(32)
	global_store_dwordx4 v2, v[124:127], s[34:35] nt
	s_add_u32 s34, s34, 0x1000
	s_addc_u32 s35, s35, 0
	s_waitcnt vmcnt(31)
	global_store_dwordx4 v2, v[128:131], s[34:35] nt
	s_add_u32 s34, s34, 0x1000
	s_addc_u32 s35, s35, 0
	s_endpgm
.Lrg_slow:
	s_load_dwordx2 s[4:5], s[0:1], 0x28
	v_and_b32_e32 v26, 63, v0
	s_bfe_u32 s3, s2, 0x30003
	v_cmp_gt_u32_e64 s[10:11], 64, v0
	s_waitcnt lgkmcnt(0)
	s_load_dword s33, s[4:5], 0x0
	s_and_saveexec_b64 s[6:7], s[10:11]
	s_cbranch_execz .LBB2_3
	s_load_dwordx2 s[4:5], s[0:1], 0x30
	v_lshlrev_b32_e32 v1, 5, v0
	v_lshl_or_b32 v1, s3, 11, v1
	s_waitcnt lgkmcnt(0)
	global_load_dwordx4 v[8:11], v1, s[4:5]
	global_load_dwordx4 v[2:5], v1, s[4:5] offset:16
	v_mov_b32_e32 v1, s33
	s_waitcnt vmcnt(1)
	v_mov_b32_e32 v6, v8
	s_waitcnt vmcnt(0)
	v_mov_b32_e32 v7, v2
	v_mov_b32_e32 v2, v9
	v_mov_b32_e32 v8, v10
	v_mov_b32_e32 v9, v4
	v_mov_b32_e32 v4, v11
	v_pk_add_f32 v[2:3], v[6:7], v[2:3]
	v_pk_add_f32 v[4:5], v[8:9], v[4:5]
	s_nop 0
	v_pk_add_f32 v[2:3], v[2:3], v[4:5]
	s_nop 0
	v_add_f32_e32 v2, v2, v3
	v_fmamk_f32 v1, v2, 0x3c800000, v1
	v_add_f32_e32 v2, 0xba03126f, v1
	v_readlane_b32 s5, v1, 1
	v_add_f32_e32 v3, 0x3a03126f, v1
	v_readlane_b32 s8, v1, 2
	v_cmp_ge_f32_e32 vcc, s5, v2
	v_readlane_b32 s12, v1, 4
	v_readlane_b32 s14, v1, 6
	v_cndmask_b32_e64 v4, 0, 1, vcc
	v_cmp_gt_f32_e32 vcc, s5, v3
	v_readlane_b32 s16, v1, 8
	v_readlane_b32 s18, v1, 10
	v_cndmask_b32_e64 v5, 0, 1, vcc
	v_cmp_ge_f32_e32 vcc, s8, v2
	v_readlane_b32 s20, v1, 12
	v_readlane_b32 s4, v1, 0
	v_cndmask_b32_e64 v6, 0, 1, vcc
	v_cmp_gt_f32_e32 vcc, s8, v3
	v_readlane_b32 s9, v1, 3
	v_readlane_b32 s13, v1, 5
	v_cndmask_b32_e64 v7, 0, 1, vcc
	v_cmp_ge_f32_e32 vcc, s12, v2
	v_readlane_b32 s15, v1, 7
	v_readlane_b32 s17, v1, 9
	v_cndmask_b32_e64 v8, 0, 1, vcc
	v_cmp_gt_f32_e32 vcc, s12, v3
	v_readlane_b32 s19, v1, 11
	v_readlane_b32 s21, v1, 13
	v_cndmask_b32_e64 v9, 0, 1, vcc
	v_cmp_ge_f32_e32 vcc, s14, v2
	s_nop 1
	v_cndmask_b32_e64 v10, 0, 1, vcc
	v_cmp_gt_f32_e32 vcc, s14, v3
	s_nop 1
	v_cndmask_b32_e64 v11, 0, 1, vcc
	v_cmp_ge_f32_e32 vcc, s16, v2
	s_nop 1
	v_cndmask_b32_e64 v12, 0, 1, vcc
	v_cmp_gt_f32_e32 vcc, s16, v3
	s_nop 1
	v_cndmask_b32_e64 v13, 0, 1, vcc
	v_cmp_ge_f32_e32 vcc, s18, v2
	s_nop 1
	v_cndmask_b32_e64 v14, 0, 1, vcc
	v_cmp_gt_f32_e32 vcc, s18, v3
	s_nop 1
	v_cndmask_b32_e64 v15, 0, 1, vcc
	v_cmp_ge_f32_e32 vcc, s20, v2
	s_nop 1
	v_cndmask_b32_e64 v16, 0, 1, vcc
	v_cmp_gt_f32_e32 vcc, s20, v3
	s_nop 1
	v_cndmask_b32_e64 v17, 0, 1, vcc
	v_cmp_ge_f32_e32 vcc, s4, v2
	s_nop 1
	v_addc_co_u32_e32 v4, vcc, 0, v4, vcc
	v_cmp_gt_f32_e32 vcc, s4, v3
	v_readlane_b32 s4, v1, 14
	s_nop 0
	v_addc_co_u32_e32 v5, vcc, 0, v5, vcc
	v_cmp_ge_f32_e32 vcc, s9, v2
	s_nop 1
	v_addc_co_u32_e32 v4, vcc, v4, v6, vcc
	v_cmp_gt_f32_e32 vcc, s9, v3
	s_nop 1
	v_addc_co_u32_e32 v5, vcc, v5, v7, vcc
	v_cmp_ge_f32_e32 vcc, s13, v2
	s_nop 1
	v_addc_co_u32_e32 v4, vcc, v4, v8, vcc
	v_cmp_gt_f32_e32 vcc, s13, v3
	s_nop 1
	v_addc_co_u32_e32 v5, vcc, v5, v9, vcc
	v_cmp_ge_f32_e32 vcc, s15, v2
	s_nop 1
	v_addc_co_u32_e32 v4, vcc, v4, v10, vcc
	v_cmp_gt_f32_e32 vcc, s15, v3
	s_nop 1
	v_addc_co_u32_e32 v5, vcc, v5, v11, vcc
	v_cmp_ge_f32_e32 vcc, s17, v2
	s_nop 1
	v_addc_co_u32_e32 v4, vcc, v4, v12, vcc
	v_cmp_gt_f32_e32 vcc, s17, v3
	s_nop 1
	v_addc_co_u32_e32 v5, vcc, v5, v13, vcc
	v_cmp_ge_f32_e32 vcc, s19, v2
	s_nop 1
	v_addc_co_u32_e32 v4, vcc, v4, v14, vcc
	v_cmp_gt_f32_e32 vcc, s19, v3
	s_nop 1
	v_addc_co_u32_e32 v5, vcc, v5, v15, vcc
	v_cmp_ge_f32_e32 vcc, s21, v2
	s_nop 1
	v_addc_co_u32_e32 v4, vcc, v4, v16, vcc
	v_cmp_gt_f32_e32 vcc, s21, v3
	s_nop 1
	v_addc_co_u32_e32 v5, vcc, v5, v17, vcc
	v_cmp_ge_f32_e32 vcc, s4, v2
	s_nop 1
	v_cndmask_b32_e64 v6, 0, 1, vcc
	v_cmp_gt_f32_e32 vcc, s4, v3
	v_readlane_b32 s4, v1, 15
	s_nop 0
	v_cndmask_b32_e64 v7, 0, 1, vcc
	v_cmp_ge_f32_e32 vcc, s4, v2
	s_nop 1
	v_addc_co_u32_e32 v4, vcc, v4, v6, vcc
	v_cmp_gt_f32_e32 vcc, s4, v3
	v_readlane_b32 s4, v1, 16
	s_nop 0
	v_addc_co_u32_e32 v5, vcc, v5, v7, vcc
	v_cmp_ge_f32_e32 vcc, s4, v2
	s_nop 1
	v_cndmask_b32_e64 v6, 0, 1, vcc
	v_cmp_gt_f32_e32 vcc, s4, v3
	v_readlane_b32 s4, v1, 17
	s_nop 0
	v_cndmask_b32_e64 v7, 0, 1, vcc
	v_cmp_ge_f32_e32 vcc, s4, v2
	s_nop 1
	v_addc_co_u32_e32 v4, vcc, v4, v6, vcc
	v_cmp_gt_f32_e32 vcc, s4, v3
	v_readlane_b32 s4, v1, 18
	s_nop 0
	v_addc_co_u32_e32 v5, vcc, v5, v7, vcc
	v_cmp_ge_f32_e32 vcc, s4, v2
	s_nop 1
	v_cndmask_b32_e64 v6, 0, 1, vcc
	v_cmp_gt_f32_e32 vcc, s4, v3
	v_readlane_b32 s4, v1, 19
	s_nop 0
	v_cndmask_b32_e64 v7, 0, 1, vcc
	v_cmp_ge_f32_e32 vcc, s4, v2
	s_nop 1
	v_addc_co_u32_e32 v4, vcc, v4, v6, vcc
	v_cmp_gt_f32_e32 vcc, s4, v3
	v_readlane_b32 s4, v1, 20
	s_nop 0
	v_addc_co_u32_e32 v5, vcc, v5, v7, vcc
	v_cmp_ge_f32_e32 vcc, s4, v2
	s_nop 1
	v_cndmask_b32_e64 v6, 0, 1, vcc
	v_cmp_gt_f32_e32 vcc, s4, v3
	v_readlane_b32 s4, v1, 21
	s_nop 0
	v_cndmask_b32_e64 v7, 0, 1, vcc
	v_cmp_ge_f32_e32 vcc, s4, v2
	s_nop 1
	v_addc_co_u32_e32 v4, vcc, v4, v6, vcc
	v_cmp_gt_f32_e32 vcc, s4, v3
	v_readlane_b32 s4, v1, 22
	s_nop 0
	v_addc_co_u32_e32 v5, vcc, v5, v7, vcc
	v_cmp_ge_f32_e32 vcc, s4, v2
	s_nop 1
	v_cndmask_b32_e64 v6, 0, 1, vcc
	v_cmp_gt_f32_e32 vcc, s4, v3
	v_readlane_b32 s4, v1, 23
	s_nop 0
	v_cndmask_b32_e64 v7, 0, 1, vcc
	v_cmp_ge_f32_e32 vcc, s4, v2
	s_nop 1
	v_addc_co_u32_e32 v4, vcc, v4, v6, vcc
	v_cmp_gt_f32_e32 vcc, s4, v3
	v_readlane_b32 s4, v1, 24
	s_nop 0
	v_addc_co_u32_e32 v5, vcc, v5, v7, vcc
	v_cmp_ge_f32_e32 vcc, s4, v2
	s_nop 1
	v_cndmask_b32_e64 v6, 0, 1, vcc
	v_cmp_gt_f32_e32 vcc, s4, v3
	v_readlane_b32 s4, v1, 25
	s_nop 0
	v_cndmask_b32_e64 v7, 0, 1, vcc
	v_cmp_ge_f32_e32 vcc, s4, v2
	s_nop 1
	v_addc_co_u32_e32 v4, vcc, v4, v6, vcc
	v_cmp_gt_f32_e32 vcc, s4, v3
	v_readlane_b32 s4, v1, 26
	s_nop 0
	v_addc_co_u32_e32 v5, vcc, v5, v7, vcc
	v_cmp_ge_f32_e32 vcc, s4, v2
	s_nop 1
	v_cndmask_b32_e64 v6, 0, 1, vcc
	v_cmp_gt_f32_e32 vcc, s4, v3
	v_readlane_b32 s4, v1, 27
	s_nop 0
	v_cndmask_b32_e64 v7, 0, 1, vcc
	v_cmp_ge_f32_e32 vcc, s4, v2
	s_nop 1
	v_addc_co_u32_e32 v4, vcc, v4, v6, vcc
	v_cmp_gt_f32_e32 vcc, s4, v3
	v_readlane_b32 s4, v1, 28
	s_nop 0
	v_addc_co_u32_e32 v5, vcc, v5, v7, vcc
	v_cmp_ge_f32_e32 vcc, s4, v2
	s_nop 1
	v_cndmask_b32_e64 v6, 0, 1, vcc
	v_cmp_gt_f32_e32 vcc, s4, v3
	v_readlane_b32 s4, v1, 29
	s_nop 0
	v_cndmask_b32_e64 v7, 0, 1, vcc
	v_cmp_ge_f32_e32 vcc, s4, v2
	s_nop 1
	v_addc_co_u32_e32 v4, vcc, v4, v6, vcc
	v_cmp_gt_f32_e32 vcc, s4, v3
	v_readlane_b32 s4, v1, 30
	s_nop 0
	v_addc_co_u32_e32 v5, vcc, v5, v7, vcc
	v_cmp_ge_f32_e32 vcc, s4, v2
	s_nop 1
	v_cndmask_b32_e64 v6, 0, 1, vcc
	v_cmp_gt_f32_e32 vcc, s4, v3
	v_readlane_b32 s4, v1, 31
	s_nop 0
	v_cndmask_b32_e64 v7, 0, 1, vcc
	v_cmp_ge_f32_e32 vcc, s4, v2
	s_nop 1
	v_addc_co_u32_e32 v4, vcc, v4, v6, vcc
	v_cmp_gt_f32_e32 vcc, s4, v3
	v_readlane_b32 s4, v1, 32
	s_nop 0
	v_addc_co_u32_e32 v5, vcc, v5, v7, vcc
	v_cmp_ge_f32_e32 vcc, s4, v2
	s_nop 1
	v_cndmask_b32_e64 v6, 0, 1, vcc
	v_cmp_gt_f32_e32 vcc, s4, v3
	v_readlane_b32 s4, v1, 33
	s_nop 0
	v_cndmask_b32_e64 v7, 0, 1, vcc
	v_cmp_ge_f32_e32 vcc, s4, v2
	s_nop 1
	v_addc_co_u32_e32 v4, vcc, v4, v6, vcc
	v_cmp_gt_f32_e32 vcc, s4, v3
	v_readlane_b32 s4, v1, 34
	s_nop 0
	v_addc_co_u32_e32 v5, vcc, v5, v7, vcc
	v_cmp_ge_f32_e32 vcc, s4, v2
	s_nop 1
	v_cndmask_b32_e64 v6, 0, 1, vcc
	v_cmp_gt_f32_e32 vcc, s4, v3
	v_readlane_b32 s4, v1, 35
	s_nop 0
	v_cndmask_b32_e64 v7, 0, 1, vcc
	v_cmp_ge_f32_e32 vcc, s4, v2
	s_nop 1
	v_addc_co_u32_e32 v4, vcc, v4, v6, vcc
	v_cmp_gt_f32_e32 vcc, s4, v3
	v_readlane_b32 s4, v1, 36
	s_nop 0
	v_addc_co_u32_e32 v5, vcc, v5, v7, vcc
	v_cmp_ge_f32_e32 vcc, s4, v2
	s_nop 1
	v_cndmask_b32_e64 v6, 0, 1, vcc
	v_cmp_gt_f32_e32 vcc, s4, v3
	v_readlane_b32 s4, v1, 37
	s_nop 0
	v_cndmask_b32_e64 v7, 0, 1, vcc
	v_cmp_ge_f32_e32 vcc, s4, v2
	s_nop 1
	v_addc_co_u32_e32 v4, vcc, v4, v6, vcc
	v_cmp_gt_f32_e32 vcc, s4, v3
	v_readlane_b32 s4, v1, 38
	s_nop 0
	v_addc_co_u32_e32 v5, vcc, v5, v7, vcc
	v_cmp_ge_f32_e32 vcc, s4, v2
	s_nop 1
	v_cndmask_b32_e64 v6, 0, 1, vcc
	v_cmp_gt_f32_e32 vcc, s4, v3
	v_readlane_b32 s4, v1, 39
	s_nop 0
	v_cndmask_b32_e64 v7, 0, 1, vcc
	v_cmp_ge_f32_e32 vcc, s4, v2
	s_nop 1
	v_addc_co_u32_e32 v4, vcc, v4, v6, vcc
	v_cmp_gt_f32_e32 vcc, s4, v3
	v_readlane_b32 s4, v1, 40
	s_nop 0
	v_addc_co_u32_e32 v5, vcc, v5, v7, vcc
	v_cmp_ge_f32_e32 vcc, s4, v2
	s_nop 1
	v_cndmask_b32_e64 v6, 0, 1, vcc
	v_cmp_gt_f32_e32 vcc, s4, v3
	v_readlane_b32 s4, v1, 41
	s_nop 0
	v_cndmask_b32_e64 v7, 0, 1, vcc
	v_cmp_ge_f32_e32 vcc, s4, v2
	s_nop 1
	v_addc_co_u32_e32 v4, vcc, v4, v6, vcc
	v_cmp_gt_f32_e32 vcc, s4, v3
	v_readlane_b32 s4, v1, 42
	s_nop 0
	v_addc_co_u32_e32 v5, vcc, v5, v7, vcc
	v_cmp_ge_f32_e32 vcc, s4, v2
	s_nop 1
	v_cndmask_b32_e64 v6, 0, 1, vcc
	v_cmp_gt_f32_e32 vcc, s4, v3
	v_readlane_b32 s4, v1, 43
	s_nop 0
	v_cndmask_b32_e64 v7, 0, 1, vcc
	v_cmp_ge_f32_e32 vcc, s4, v2
	s_nop 1
	v_addc_co_u32_e32 v4, vcc, v4, v6, vcc
	v_cmp_gt_f32_e32 vcc, s4, v3
	v_readlane_b32 s4, v1, 44
	s_nop 0
	v_addc_co_u32_e32 v5, vcc, v5, v7, vcc
	v_cmp_ge_f32_e32 vcc, s4, v2
	s_nop 1
	v_cndmask_b32_e64 v6, 0, 1, vcc
	v_cmp_gt_f32_e32 vcc, s4, v3
	v_readlane_b32 s4, v1, 45
	s_nop 0
	v_cndmask_b32_e64 v7, 0, 1, vcc
	v_cmp_ge_f32_e32 vcc, s4, v2
	s_nop 1
	v_addc_co_u32_e32 v4, vcc, v4, v6, vcc
	v_cmp_gt_f32_e32 vcc, s4, v3
	v_readlane_b32 s4, v1, 46
	s_nop 0
	v_addc_co_u32_e32 v5, vcc, v5, v7, vcc
	v_cmp_ge_f32_e32 vcc, s4, v2
	s_nop 1
	v_cndmask_b32_e64 v6, 0, 1, vcc
	v_cmp_gt_f32_e32 vcc, s4, v3
	v_readlane_b32 s4, v1, 47
	s_nop 0
	v_cndmask_b32_e64 v7, 0, 1, vcc
	v_cmp_ge_f32_e32 vcc, s4, v2
	s_nop 1
	v_addc_co_u32_e32 v4, vcc, v4, v6, vcc
	v_cmp_gt_f32_e32 vcc, s4, v3
	v_readlane_b32 s4, v1, 48
	s_nop 0
	v_addc_co_u32_e32 v5, vcc, v5, v7, vcc
	v_cmp_ge_f32_e32 vcc, s4, v2
	s_nop 1
	v_cndmask_b32_e64 v6, 0, 1, vcc
	v_cmp_gt_f32_e32 vcc, s4, v3
	v_readlane_b32 s4, v1, 49
	s_nop 0
	v_cndmask_b32_e64 v7, 0, 1, vcc
	v_cmp_ge_f32_e32 vcc, s4, v2
	s_nop 1
	v_addc_co_u32_e32 v4, vcc, v4, v6, vcc
	v_cmp_gt_f32_e32 vcc, s4, v3
	v_readlane_b32 s4, v1, 50
	s_nop 0
	v_addc_co_u32_e32 v5, vcc, v5, v7, vcc
	v_cmp_ge_f32_e32 vcc, s4, v2
	s_nop 1
	v_cndmask_b32_e64 v6, 0, 1, vcc
	v_cmp_gt_f32_e32 vcc, s4, v3
	v_readlane_b32 s4, v1, 51
	s_nop 0
	v_cndmask_b32_e64 v7, 0, 1, vcc
	v_cmp_ge_f32_e32 vcc, s4, v2
	s_nop 1
	v_addc_co_u32_e32 v4, vcc, v4, v6, vcc
	v_cmp_gt_f32_e32 vcc, s4, v3
	v_readlane_b32 s4, v1, 52
	s_nop 0
	v_addc_co_u32_e32 v5, vcc, v5, v7, vcc
	v_cmp_ge_f32_e32 vcc, s4, v2
	s_nop 1
	v_cndmask_b32_e64 v6, 0, 1, vcc
	v_cmp_gt_f32_e32 vcc, s4, v3
	v_readlane_b32 s4, v1, 53
	s_nop 0
	v_cndmask_b32_e64 v7, 0, 1, vcc
	v_cmp_ge_f32_e32 vcc, s4, v2
	s_nop 1
	v_addc_co_u32_e32 v4, vcc, v4, v6, vcc
	v_cmp_gt_f32_e32 vcc, s4, v3
	v_readlane_b32 s4, v1, 54
	s_nop 0
	v_addc_co_u32_e32 v5, vcc, v5, v7, vcc
	v_cmp_ge_f32_e32 vcc, s4, v2
	s_nop 1
	v_cndmask_b32_e64 v6, 0, 1, vcc
	v_cmp_gt_f32_e32 vcc, s4, v3
	v_readlane_b32 s4, v1, 55
	s_nop 0
	v_cndmask_b32_e64 v7, 0, 1, vcc
	v_cmp_ge_f32_e32 vcc, s4, v2
	s_nop 1
	v_addc_co_u32_e32 v4, vcc, v4, v6, vcc
	v_cmp_gt_f32_e32 vcc, s4, v3
	v_readlane_b32 s4, v1, 56
	s_nop 0
	v_addc_co_u32_e32 v5, vcc, v5, v7, vcc
	v_cmp_ge_f32_e32 vcc, s4, v2
	s_nop 1
	v_cndmask_b32_e64 v6, 0, 1, vcc
	v_cmp_gt_f32_e32 vcc, s4, v3
	v_readlane_b32 s4, v1, 57
	s_nop 0
	v_cndmask_b32_e64 v7, 0, 1, vcc
	v_cmp_ge_f32_e32 vcc, s4, v2
	s_nop 1
	v_addc_co_u32_e32 v4, vcc, v4, v6, vcc
	v_cmp_gt_f32_e32 vcc, s4, v3
	v_readlane_b32 s4, v1, 58
	s_nop 0
	v_addc_co_u32_e32 v5, vcc, v5, v7, vcc
	v_cmp_ge_f32_e32 vcc, s4, v2
	s_nop 1
	v_cndmask_b32_e64 v6, 0, 1, vcc
	v_cmp_gt_f32_e32 vcc, s4, v3
	v_readlane_b32 s4, v1, 59
	s_nop 0
	v_cndmask_b32_e64 v7, 0, 1, vcc
	v_cmp_ge_f32_e32 vcc, s4, v2
	s_nop 1
	v_addc_co_u32_e32 v4, vcc, v4, v6, vcc
	v_cmp_gt_f32_e32 vcc, s4, v3
	v_readlane_b32 s4, v1, 60
	s_nop 0
	v_addc_co_u32_e32 v5, vcc, v5, v7, vcc
	v_cmp_ge_f32_e32 vcc, s4, v2
	s_nop 1
	v_cndmask_b32_e64 v6, 0, 1, vcc
	v_cmp_gt_f32_e32 vcc, s4, v3
	v_readlane_b32 s4, v1, 61
	s_nop 0
	v_cndmask_b32_e64 v7, 0, 1, vcc
	v_cmp_ge_f32_e32 vcc, s4, v2
	s_nop 1
	v_addc_co_u32_e32 v4, vcc, v4, v6, vcc
	v_cmp_gt_f32_e32 vcc, s4, v3
	v_readlane_b32 s4, v1, 62
	s_nop 0
	v_addc_co_u32_e32 v5, vcc, v5, v7, vcc
	v_cmp_ge_f32_e32 vcc, s4, v2
	s_nop 1
	v_cndmask_b32_e64 v6, 0, 1, vcc
	v_cmp_gt_f32_e32 vcc, s4, v3
	v_readlane_b32 s4, v1, 63
	s_nop 0
	v_cndmask_b32_e64 v7, 0, 1, vcc
	v_cmp_ge_f32_e32 vcc, s4, v2
	s_nop 1
	v_addc_co_u32_e32 v1, vcc, v4, v6, vcc
	v_cmp_gt_f32_e32 vcc, s4, v3
	v_cmp_gt_u32_e64 s[8:9], 33, v1
	s_nop 0
	v_addc_co_u32_e32 v2, vcc, v5, v7, vcc
	v_cmp_lt_u32_e32 vcc, 32, v1
	v_cmp_gt_u32_e64 s[4:5], 32, v2
	s_and_b64 s[4:5], vcc, s[4:5]
	s_nop 0
	v_cndmask_b32_e64 v2, 0, 1, s[4:5]
	v_cmp_ne_u32_e32 vcc, 0, v2
	v_cmp_eq_u32_e64 s[4:5], 0, v26
	s_and_b64 exec, exec, s[4:5]
	s_cbranch_execz .LBB2_3
	v_mov_b32_e32 v2, s8
	v_mov_b32_e32 v3, s9
	v_mov_b32_e32 v4, vcc_lo
	v_mov_b32_e32 v5, vcc_hi
	v_mov_b32_e32 v1, 0
	ds_write_b128 v1, v[2:5] offset:16400

	.amdhsa_kernel _Z20refine_gather_kernelPKfS0_S0_S0_S0_S0_S0_PfPiS1_
		.amdhsa_group_segment_fixed_size 16424
		.amdhsa_private_segment_fixed_size 0
		.amdhsa_kernarg_size 80
		.amdhsa_user_sgpr_count 2
		.amdhsa_user_sgpr_dispatch_ptr 0
		.amdhsa_user_sgpr_queue_ptr 0
		.amdhsa_user_sgpr_kernarg_segment_ptr 1
		.amdhsa_user_sgpr_dispatch_id 0
		.amdhsa_user_sgpr_kernarg_preload_length 0
		.amdhsa_user_sgpr_kernarg_preload_offset 0
		.amdhsa_user_sgpr_private_segment_size 0
		.amdhsa_uses_dynamic_stack 0
		.amdhsa_enable_private_segment 0
		.amdhsa_system_sgpr_workgroup_id_x 1
		.amdhsa_system_sgpr_workgroup_id_y 0
		.amdhsa_system_sgpr_workgroup_id_z 0
		.amdhsa_system_sgpr_workgroup_info 0
		.amdhsa_system_vgpr_workitem_id 0
		.amdhsa_next_free_vgpr 148
		.amdhsa_next_free_sgpr 100
		.amdhsa_accum_offset 132
		.amdhsa_reserve_vcc 1
		.amdhsa_float_round_mode_32 0
		.amdhsa_float_round_mode_16_64 0
		.amdhsa_float_denorm_mode_32 3
		.amdhsa_float_denorm_mode_16_64 3
		.amdhsa_dx10_clamp 1
		.amdhsa_ieee_mode 1
		.amdhsa_fp16_overflow 0
		.amdhsa_tg_split 0
		.amdhsa_exception_fp_ieee_invalid_op 0
		.amdhsa_exception_fp_denorm_src 0
		.amdhsa_exception_fp_ieee_div_zero 0
		.amdhsa_exception_fp_ieee_overflow 0
		.amdhsa_exception_fp_ieee_underflow 0
		.amdhsa_exception_fp_ieee_inexact 0
		.amdhsa_exception_int_div_zero 0
	.end_amdhsa_kernel

amdhsa.kernels:
  - .agpr_count:     0
    .args:
      - .actual_access:  read_only
        .address_space:  global
        .offset:         0
        .size:           8
        .value_kind:     global_buffer
      - .actual_access:  write_only
        .address_space:  global
        .offset:         8
        .size:           8
        .value_kind:     global_buffer
    .group_segment_fixed_size: 0
    .kernarg_segment_align: 8
    .kernarg_segment_size: 16
    .language:       OpenCL C
    .language_version:
      - 2
      - 0
    .max_flat_workgroup_size: 256
    .name:           _Z7prep_w1PKfPDv8_DF16_
    .private_segment_fixed_size: 0
    .sgpr_count:     14
    .sgpr_spill_count: 0
    .symbol:         _Z7prep_w1PKfPDv8_DF16_.kd
    .uniform_work_group_size: 1
    .uses_dynamic_stack: false
    .vgpr_count:     26
    .vgpr_spill_count: 0
    .wavefront_size: 64
  - .agpr_count:     0
    .args:
      - .address_space:  global
        .offset:         0
        .size:           8
        .value_kind:     global_buffer
      - .address_space:  global
        .offset:         8
        .size:           8
        .value_kind:     global_buffer
      - .address_space:  global
        .offset:         16
        .size:           8
        .value_kind:     global_buffer
      - .actual_access:  read_only
        .address_space:  global
        .offset:         24
        .size:           8
        .value_kind:     global_buffer
      - .actual_access:  read_only
        .address_space:  global
        .offset:         32
        .size:           8
        .value_kind:     global_buffer
      - .actual_access:  write_only
        .address_space:  global
        .offset:         40
        .size:           8
        .value_kind:     global_buffer
      - .actual_access:  write_only
        .address_space:  global
        .offset:         48
        .size:           8
        .value_kind:     global_buffer
    .group_segment_fixed_size: 163840
    .kernarg_segment_align: 8
    .kernarg_segment_size: 56
    .language:       OpenCL C
    .language_version:
      - 2
      - 0
    .max_flat_workgroup_size: 768
    .name:           _Z12score_kernelPKfS0_PKcS0_S0_PfPi
    .private_segment_fixed_size: 0
    .sgpr_count:     34
    .sgpr_spill_count: 0
    .symbol:         _Z12score_kernelPKfS0_PKcS0_S0_PfPi.kd
    .uniform_work_group_size: 1
    .uses_dynamic_stack: false
    .vgpr_count:     164
    .vgpr_spill_count: 0
    .wavefront_size: 64
  - .agpr_count:     16
    .args:
      - .actual_access:  read_only
        .address_space:  global
        .offset:         0
        .size:           8
        .value_kind:     global_buffer
      - .actual_access:  read_only
        .address_space:  global
        .offset:         8
        .size:           8
        .value_kind:     global_buffer
      - .actual_access:  read_only
        .address_space:  global
        .offset:         16
        .size:           8
        .value_kind:     global_buffer
      - .actual_access:  read_only
        .address_space:  global
        .offset:         24
        .size:           8
        .value_kind:     global_buffer
      - .actual_access:  read_only
        .address_space:  global
        .offset:         32
        .size:           8
        .value_kind:     global_buffer
      - .actual_access:  read_only
        .address_space:  global
        .offset:         40
        .size:           8
        .value_kind:     global_buffer
      - .actual_access:  read_only
        .address_space:  global
        .offset:         48
        .size:           8
        .value_kind:     global_buffer
      - .address_space:  global
        .offset:         56
        .size:           8
        .value_kind:     global_buffer
      - .address_space:  global
        .offset:         64
        .size:           8
        .value_kind:     global_buffer
      - .actual_access:  write_only
        .address_space:  global
        .offset:         72
        .size:           8
        .value_kind:     global_buffer
    .group_segment_fixed_size: 16424
    .kernarg_segment_align: 8
    .kernarg_segment_size: 80
    .language:       OpenCL C
    .language_version:
      - 2
      - 0
    .max_flat_workgroup_size: 256
    .name:           _Z20refine_gather_kernelPKfS0_S0_S0_S0_S0_S0_PfPiS1_
    .private_segment_fixed_size: 0
    .sgpr_count:     106
    .sgpr_spill_count: 94
    .symbol:         _Z20refine_gather_kernelPKfS0_S0_S0_S0_S0_S0_PfPiS1_.kd
    .uniform_work_group_size: 1
    .uses_dynamic_stack: false
    .vgpr_count:     148
    .vgpr_spill_count: 0
    .wavefront_size: 64
